# speedup vs baseline: 1.0161x; 1.0161x over previous
.LBB1_4:
	s_or_b64 exec, exec, s[4:5]
	s_load_dwordx2 s[26:27], s[0:1], 0x8
	s_load_dwordx4 s[28:31], s[0:1], 0x18
	s_load_dwordx2 s[36:37], s[0:1], 0x30
	v_and_b32_e32 v18, 7, v0
	s_movk_i32 s4, 0x3e8
	v_cmp_gt_u32_e32 vcc, s4, v0
	v_cmp_eq_u32_e64 s[4:5], 0, v18
	s_waitcnt vmcnt(4)
	v_mov_b32_e32 v21, v58
	v_mov_b32_e32 v27, v59
	v_sub_u32_e32 v19, v27, v21
	s_and_b64 s[4:5], s[4:5], vcc
	s_waitcnt lgkmcnt(0)
	s_barrier
	s_load_dwordx2 s[34:35], s[0:1], 0x28
	s_movk_i32 s0, 0x1400
	v_mad_u32_u24 v27, v20, s0, v21
	v_add_u32_e32 v20, v18, v27
	v_min_u32_e32 v20, 0x9c3ff, v20
	v_or_b32_e32 v31, 8, v18
	v_lshlrev_b32_e32 v29, 2, v20
	v_add_u32_e32 v20, v31, v27
	v_min_u32_e32 v20, 0x9c3ff, v20
	v_or_b32_e32 v30, 16, v18
	v_lshlrev_b32_e32 v35, 2, v20
	v_add_u32_e32 v20, v30, v27
	v_min_u32_e32 v20, 0x9c3ff, v20
	v_lshlrev_b32_e32 v36, 2, v20
	v_or_b32_e32 v20, 24, v18
	v_add_u32_e32 v21, v20, v27
	v_min_u32_e32 v21, 0x9c3ff, v21
	v_lshlrev_b32_e32 v37, 2, v21
	global_load_dword v38, v29, s[26:27]
	global_load_dword v34, v35, s[26:27]
	global_load_dword v33, v36, s[26:27]
	global_load_dword v21, v37, s[26:27]
	s_mov_b32 s11, 0
	s_and_saveexec_b64 s[6:7], s[4:5]
	s_cbranch_execz .LBB1_13
	s_mov_b64 s[4:5], exec
.LBB1_6:
	s_ff1_i32_b64 s10, s[4:5]
	v_readlane_b32 s14, v58, s10
	s_lshl_b64 s[12:13], 1, s10
	s_add_i32 s11, s11, s14
	s_andn2_b64 s[4:5], s[4:5], s[12:13]
	s_cmp_lg_u64 s[4:5], 0
	s_cbranch_scc1 .LBB1_6
	v_mbcnt_lo_u32_b32 v60, exec_lo, 0
	v_mbcnt_hi_u32_b32 v60, exec_hi, v60
	s_mov_b32 s10, 0
	v_cmp_eq_u32_e64 s[4:5], 0, v60
	s_and_saveexec_b64 s[12:13], s[4:5]
	s_xor_b64 s[4:5], exec, s[12:13]
	v_mov_b32_e32 v60, 0
	v_mov_b32_e32 v61, s11
	ds_add_u32 v60, v61 offset:22528
	s_or_b64 exec, exec, s[4:5]
	s_mov_b64 s[4:5], exec
.LBB1_10:
	s_ff1_i32_b64 s11, s[4:5]
	v_readlane_b32 s14, v19, s11
	s_lshl_b64 s[12:13], 1, s11
	s_add_i32 s10, s10, s14
	s_andn2_b64 s[4:5], s[4:5], s[12:13]
	s_cmp_lg_u64 s[4:5], 0
	s_cbranch_scc1 .LBB1_10
	v_mbcnt_lo_u32_b32 v60, exec_lo, 0
	v_mbcnt_hi_u32_b32 v60, exec_hi, v60
	v_cmp_eq_u32_e64 s[4:5], 0, v60
	s_and_saveexec_b64 s[12:13], s[4:5]
	s_xor_b64 s[12:13], exec, s[12:13]
	v_mov_b32_e32 v60, 0
	v_mov_b32_e32 v61, s10
	ds_add_u32 v60, v61 offset:22532
.LBB1_13:
	s_or_b64 exec, exec, s[6:7]
	v_cndmask_b32_e32 v29, 0, v19, vcc
	v_cmp_lt_u32_e32 vcc, v18, v29
	s_waitcnt vmcnt(3)
	s_nop 0
	v_cndmask_b32_e32 v37, -1, v38, vcc
	v_cmp_ne_u32_e64 s[6:7], -1, v37
	s_and_saveexec_b64 s[0:1], s[6:7]
	v_mov_b32_e32 v19, 2
	v_lshlrev_b32_sdwa v19, v19, v37 dst_sel:DWORD dst_unused:UNUSED_PAD src0_sel:DWORD src1_sel:WORD_1
	v_mov_b32_e32 v35, 1
	ds_add_u32 v19, v35 offset:16384
	s_or_b64 exec, exec, s[0:1]
	v_cmp_lt_u32_e32 vcc, v31, v29
	s_waitcnt vmcnt(2)
	s_nop 0
	v_cndmask_b32_e32 v36, -1, v34, vcc
	v_cmp_ne_u32_e64 s[4:5], -1, v36
	s_and_saveexec_b64 s[0:1], s[4:5]
	v_mov_b32_e32 v19, 2
	v_lshlrev_b32_sdwa v19, v19, v36 dst_sel:DWORD dst_unused:UNUSED_PAD src0_sel:DWORD src1_sel:WORD_1
	v_mov_b32_e32 v31, 1
	ds_add_u32 v19, v31 offset:16384
	s_or_b64 exec, exec, s[0:1]
	v_cmp_lt_u32_e32 vcc, v30, v29
	s_waitcnt vmcnt(1)
	s_nop 0
	v_cndmask_b32_e32 v35, -1, v33, vcc
	v_cmp_ne_u32_e64 s[16:17], -1, v35
	s_and_saveexec_b64 s[0:1], s[16:17]
	v_mov_b32_e32 v19, 2
	v_lshlrev_b32_sdwa v19, v19, v35 dst_sel:DWORD dst_unused:UNUSED_PAD src0_sel:DWORD src1_sel:WORD_1
	v_mov_b32_e32 v30, 1
	ds_add_u32 v19, v30 offset:16384
	s_or_b64 exec, exec, s[0:1]
	v_cmp_lt_u32_e32 vcc, v20, v29
	s_waitcnt vmcnt(0)
	s_nop 0
	v_cndmask_b32_e32 v34, -1, v21, vcc
	v_cmp_ne_u32_e64 s[0:1], -1, v34
	s_and_saveexec_b64 s[10:11], s[0:1]
	v_mov_b32_e32 v19, 2
	v_lshlrev_b32_sdwa v19, v19, v34 dst_sel:DWORD dst_unused:UNUSED_PAD src0_sel:DWORD src1_sel:WORD_1
	v_mov_b32_e32 v20, 1
	ds_add_u32 v19, v20 offset:16384
	s_or_b64 exec, exec, s[10:11]
	v_or_b32_e32 v33, 32, v18
	v_cmp_lt_u32_e32 vcc, v33, v29
	s_and_saveexec_b64 s[12:13], vcc
	s_cbranch_execz .LBB1_24
	s_mov_b64 s[14:15], 0
	v_mov_b32_e32 v19, 0
	v_mov_b32_e32 v20, 1
	v_mov_b32_e32 v21, 2
	v_mov_b32_e32 v30, v33
